# grid barrier: non-leader workgroups poll the global generation word directly instead of the per-XCD word relayed by their XCD leader, on top of v017
# speedup vs baseline: 1.0123x; 1.0123x over previous
.LBB0_180:
	s_or_b64 exec, exec, s[4:5]
	v_cvt_f32_u32_e32 v6, v3
	s_waitcnt vmcnt(0)
	v_readfirstlane_b32 s4, v5
	v_sub_u32_e32 v5, 0, v3
	v_rcp_iflag_f32_e32 v6, v6
	v_add_u32_e32 v7, s4, v4
	v_mul_f32_e32 v6, 0x4f7ffffe, v6
	v_cvt_u32_f32_e32 v6, v6
	v_mul_lo_u32 v4, v5, v6
	v_mul_hi_u32 v4, v6, v4
	v_add_u32_e32 v4, v6, v4
	v_mul_hi_u32 v4, v7, v4
	v_mul_lo_u32 v5, v4, v3
	v_sub_u32_e32 v5, v7, v5
	v_add_u32_e32 v6, 1, v4
	v_cmp_ge_u32_e32 vcc, v5, v3
	s_nop 1
	v_cndmask_b32_e32 v4, v4, v6, vcc
	v_sub_u32_e32 v6, v5, v3
	v_cndmask_b32_e32 v5, v5, v6, vcc
	v_add_u32_e32 v6, 1, v4
	v_cmp_ge_u32_e32 vcc, v5, v3
	v_add_u32_e32 v5, 1, v7
	s_nop 0
	v_cndmask_b32_e32 v4, v4, v6, vcc
	v_mul_lo_u32 v6, v3, v4
	v_add_u32_e32 v3, v6, v3
	v_cmp_ne_u32_e32 vcc, v5, v3
	s_and_saveexec_b64 s[4:5], vcc
	s_xor_b64 s[4:5], exec, s[4:5]
	s_cbranch_execz .LBB0_194
	v_readlane_b32 s6, v254, 20
	v_readlane_b32 s7, v254, 21
	s_waitcnt lgkmcnt(0)
	s_nop 3
	global_load_dword v2, v207, s[6:7] sc1
	s_waitcnt vmcnt(0)
	v_cmp_eq_u32_e32 vcc, v2, v4
	s_and_saveexec_b64 s[6:7], vcc
	s_cbranch_execz .LBB0_193
	s_mov_b32 s23, 1
	s_mov_b64 s[8:9], 0
	s_branch .LBB0_184

.LBB0_186:
	v_readlane_b32 s14, v254, 20
	v_readlane_b32 s15, v254, 21
	s_add_i32 s23, s23, 1
	s_mov_b64 s[16:17], -1
	s_nop 2
	global_load_dword v2, v207, s[14:15] sc1
	s_waitcnt vmcnt(0)
	v_cmp_ne_u32_e32 vcc, v2, v4
	s_orn2_b64 s[14:15], vcc, exec
	s_branch .LBB0_183

.LBB0_296:
	s_or_b64 exec, exec, s[4:5]
	v_cvt_f32_u32_e32 v6, v3
	s_waitcnt vmcnt(0)
	v_readfirstlane_b32 s4, v5
	v_sub_u32_e32 v5, 0, v3
	v_rcp_iflag_f32_e32 v6, v6
	v_add_u32_e32 v7, s4, v4
	v_mul_f32_e32 v6, 0x4f7ffffe, v6
	v_cvt_u32_f32_e32 v6, v6
	v_mul_lo_u32 v4, v5, v6
	v_mul_hi_u32 v4, v6, v4
	v_add_u32_e32 v4, v6, v4
	v_mul_hi_u32 v4, v7, v4
	v_mul_lo_u32 v5, v4, v3
	v_sub_u32_e32 v5, v7, v5
	v_add_u32_e32 v6, 1, v4
	v_cmp_ge_u32_e32 vcc, v5, v3
	s_nop 1
	v_cndmask_b32_e32 v4, v4, v6, vcc
	v_sub_u32_e32 v6, v5, v3
	v_cndmask_b32_e32 v5, v5, v6, vcc
	v_add_u32_e32 v6, 1, v4
	v_cmp_ge_u32_e32 vcc, v5, v3
	v_add_u32_e32 v5, 1, v7
	s_nop 0
	v_cndmask_b32_e32 v4, v4, v6, vcc
	v_mul_lo_u32 v6, v3, v4
	v_add_u32_e32 v3, v6, v3
	v_cmp_ne_u32_e32 vcc, v5, v3
	s_and_saveexec_b64 s[4:5], vcc
	s_xor_b64 s[4:5], exec, s[4:5]
	s_cbranch_execz .LBB0_310
	v_readlane_b32 s6, v254, 20
	v_readlane_b32 s7, v254, 21
	s_waitcnt lgkmcnt(0)
	s_nop 3
	global_load_dword v2, v207, s[6:7] sc1
	s_waitcnt vmcnt(0)
	v_cmp_eq_u32_e32 vcc, v2, v4
	s_and_saveexec_b64 s[6:7], vcc
	s_cbranch_execz .LBB0_309
	s_mov_b32 s10, 1
	s_mov_b64 s[8:9], 0
	s_branch .LBB0_300

.LBB0_302:
	v_readlane_b32 s14, v254, 20
	v_readlane_b32 s15, v254, 21
	s_add_i32 s10, s10, 1
	s_mov_b64 s[16:17], -1
	s_nop 2
	global_load_dword v2, v207, s[14:15] sc1
	s_waitcnt vmcnt(0)
	v_cmp_ne_u32_e32 vcc, v2, v4
	s_orn2_b64 s[14:15], vcc, exec
	s_branch .LBB0_299
